# P10 hand-written (indices one row ahead, expert offsets in a register, 16-byte y loads) with 4 consecutive rows per wave; on top of P2 consecutive rows + barrier early invalidate
# baseline (speedup 1.0000x reference)
; __device__ __forceinline__ void combine_row(int m, int lane, const float* __restrict__ h1, const bf16* __restrict__ y, const unsigned* __restrict__ cnt, const int* __restrict__ tok_e, const int* __restrict__ tok_p, ...
;     size_t yrow[4]; float gk[4];
; #pragma unroll
;     for (int k = 0; k < 4; ++k) {
;         const int e = tok_e[m * 4 + k]; const int off = (int)cnt[e];
;         yrow[k] = (size_t)(off + tok_p[m * 4 + k]) * D; gk[k] = gate[m * 4 + k];
;     }
;     f32x4 v[8]; float ss = 0.f;
; #pragma unroll
;     for (int j = 0; j < 8; ++j) {
;         const int idx = j * 256 + lane * 4;
;         f32x4 a = *(const f32x4*)(h1 + (size_t)m * D + idx);
; #pragma unroll
;         for (int k = 0; k < 4; ++k) { const u32x2 w = *(const u32x2*)(y + yrow[k] + idx);
; __device__ __forceinline__ void phase10() { const Ctx c = make_ctx(); PHASE_PTRS; for (int m = c.gw; m < M; m += c.NGW) combine_row(m, c.lane, h1, y, (const unsigned*)(ws + WS_CTL) + CW_OFFT, tok_e, tok_p, gate, INP(19), ka->out); }
.LBB0_1576:
	v_readlane_b32 s0, v252, 0
	v_readlane_b32 s1, v252, 1
	s_cmp_lt_i32 s0, 11
	s_cselect_b64 s[0:1], -1, 0
	s_and_b64 s[0:1], s[0:1], s[4:5]
	s_andn2_b64 vcc, exec, s[0:1]
	s_cbranch_vccnz .LBB0_1580
	s_load_dwordx4 s[4:7], s[94:95], 0x98
	s_load_dwordx2 s[14:15], s[94:95], 0xa8
	v_and_b32_e32 v1, 63, v0
	v_readfirstlane_b32 s8, v0
	s_lshr_b32 s8, s8, 6
	s_lshl_b32 s9, s2, 3
	s_add_i32 s8, s8, s9
	s_lshl_b32 s9, s3, 3
	s_mov_b32 s66, 1
.Lp10_rpw:
	s_mul_i32 s67, s66, s9
	s_cmpk_lt_u32 s67, 0x2000
	s_cbranch_scc0 .Lp10_rpw_done
	s_add_i32 s66, s66, 1
	s_branch .Lp10_rpw
.Lp10_rpw_done:
	s_mul_i32 s8, s8, s66
	s_add_i32 s66, s8, s66
	s_min_i32 s66, s66, 0x2000
	s_cmp_lt_i32 s8, s66
	s_cbranch_scc0 .LBB0_1580
	v_lshlrev_b32_e32 v2, 5, v1
	v_lshlrev_b32_e32 v3, 4, v1
	v_lshlrev_b32_e32 v4, 2, v1
	v_mov_b32_e32 v5, 0
	v_mov_b32_e32 v157, 0x358637bd
	s_waitcnt lgkmcnt(0)
	s_add_u32 s16, s14, 0x41e00000
	s_addc_u32 s17, s15, 0
	s_add_u32 s18, s14, 0x47e00000
	s_addc_u32 s19, s15, 0
	s_add_u32 s20, s14, 0x47f00000
	s_addc_u32 s21, s15, 0
	s_add_u32 s22, s14, 0x48000000
	s_addc_u32 s23, s15, 0
	s_add_u32 s24, s14, 0x52400000
	s_addc_u32 s25, s15, 0
	s_add_u32 s10, s14, 0x1700
	s_addc_u32 s11, s15, 0
	s_add_u32 s12, s4, 0x1000
	s_addc_u32 s13, s5, 0
	s_lshl_b32 s60, s8, 4
	s_add_u32 s52, s18, s60
	s_addc_u32 s53, s19, 0
	s_add_u32 s54, s20, s60
	s_addc_u32 s55, s21, 0
	s_add_u32 s56, s22, s60
	s_addc_u32 s57, s23, 0
	global_load_dwordx4 v[40:43], v5, s[52:53]
	global_load_dwordx4 v[44:47], v5, s[54:55]
	global_load_dwordx4 v[48:51], v5, s[56:57]
	global_load_dword v6, v4, s[10:11]
	global_load_dwordx4 v[8:11], v2, s[4:5]
	global_load_dwordx4 v[12:15], v2, s[4:5] offset:16
	global_load_dwordx4 v[16:19], v2, s[4:5] offset:2048
	global_load_dwordx4 v[20:23], v2, s[4:5] offset:2064
	global_load_dwordx4 v[24:27], v2, s[12:13]
	global_load_dwordx4 v[28:31], v2, s[12:13] offset:16
	global_load_dwordx4 v[32:35], v2, s[12:13] offset:2048
	global_load_dwordx4 v[36:39], v2, s[12:13] offset:2064
	s_waitcnt vmcnt(0)
	v_readfirstlane_b32 s28, v40
	v_readfirstlane_b32 s29, v41
	v_readfirstlane_b32 s30, v42
	v_readfirstlane_b32 s31, v43
	v_readfirstlane_b32 s32, v44
	v_readfirstlane_b32 s33, v45
	v_readfirstlane_b32 s34, v46
	v_readfirstlane_b32 s35, v47
	v_readfirstlane_b32 s36, v48
	v_readfirstlane_b32 s37, v49
	v_readfirstlane_b32 s38, v50
	v_readfirstlane_b32 s39, v51
	s_nop 3
	v_readlane_b32 s60, v6, s28
	v_readlane_b32 s61, v6, s29
	v_readlane_b32 s62, v6, s30
	v_readlane_b32 s63, v6, s31
	s_add_i32 s60, s60, s32
	s_lshl_b32 s60, s60, 12
	s_add_u32 s40, s24, s60
	s_addc_u32 s41, s25, 0
	s_add_i32 s61, s61, s33
	s_lshl_b32 s61, s61, 12
	s_add_u32 s42, s24, s61
	s_addc_u32 s43, s25, 0
	s_add_i32 s62, s62, s34
	s_lshl_b32 s62, s62, 12
	s_add_u32 s44, s24, s62
	s_addc_u32 s45, s25, 0
	s_add_i32 s63, s63, s35
	s_lshl_b32 s63, s63, 12
	s_add_u32 s46, s24, s63
	s_addc_u32 s47, s25, 0
	s_lshl_b32 s60, s8, 13
	s_add_u32 s48, s16, s60
	s_addc_u32 s49, s17, 0
	s_add_u32 s58, s48, 0x1000
	s_addc_u32 s59, s49, 0
	s_add_u32 s50, s6, s60
	s_addc_u32 s51, s7, 0
	s_add_u32 s26, s50, 0x1000
	s_addc_u32 s27, s51, 0
.Lp10_loop:
	global_load_dwordx4 v[52:55], v2, s[48:49]
	global_load_dwordx4 v[56:59], v2, s[48:49] offset:16
	global_load_dwordx4 v[60:63], v2, s[48:49] offset:2048
	global_load_dwordx4 v[64:67], v2, s[48:49] offset:2064
	global_load_dwordx4 v[68:71], v2, s[58:59]
	global_load_dwordx4 v[72:75], v2, s[58:59] offset:16
	global_load_dwordx4 v[76:79], v2, s[58:59] offset:2048
	global_load_dwordx4 v[80:83], v2, s[58:59] offset:2064
	global_load_dwordx4 v[84:87], v3, s[40:41]
	global_load_dwordx4 v[88:91], v3, s[40:41] offset:1024
	global_load_dwordx4 v[92:95], v3, s[40:41] offset:2048
	global_load_dwordx4 v[96:99], v3, s[40:41] offset:3072
	global_load_dwordx4 v[100:103], v3, s[42:43]
	global_load_dwordx4 v[104:107], v3, s[42:43] offset:1024
	global_load_dwordx4 v[108:111], v3, s[42:43] offset:2048
	global_load_dwordx4 v[112:115], v3, s[42:43] offset:3072
	global_load_dwordx4 v[116:119], v3, s[44:45]
	global_load_dwordx4 v[120:123], v3, s[44:45] offset:1024
	global_load_dwordx4 v[124:127], v3, s[44:45] offset:2048
	global_load_dwordx4 v[128:131], v3, s[44:45] offset:3072
	global_load_dwordx4 v[132:135], v3, s[46:47]
	global_load_dwordx4 v[136:139], v3, s[46:47] offset:1024
	global_load_dwordx4 v[140:143], v3, s[46:47] offset:2048
	global_load_dwordx4 v[144:147], v3, s[46:47] offset:3072
	s_mov_b32 s64, s8
	s_add_i32 s8, s8, 1
	s_cmp_lt_i32 s8, s66
	s_cselect_b32 s65, 1, 0
	s_cbranch_scc0 .Lp10_noidx
	s_lshl_b32 s60, s8, 4
	s_add_u32 s52, s18, s60
	s_addc_u32 s53, s19, 0
	s_add_u32 s54, s20, s60
	s_addc_u32 s55, s21, 0
	s_add_u32 s56, s22, s60
	s_addc_u32 s57, s23, 0
	global_load_dwordx4 v[40:43], v5, s[52:53]
	global_load_dwordx4 v[44:47], v5, s[54:55]
	global_load_dwordx4 v[48:51], v5, s[56:57]
; __device__ __forceinline__ void combine_row(int m, int lane, const float* __restrict__ h1, const bf16* __restrict__ y, const unsigned* __restrict__ cnt, const int* __restrict__ tok_e, const int* __restrict__ tok_p, ...
;     ...
; #pragma unroll
;     for (int j = 0; j < 8; ++j) {
;         const int idx = j * 256 + lane * 4;
;         f32x4 a = *(const f32x4*)(h1 + (size_t)m * D + idx);
; #pragma unroll
;         for (int k = 0; k < 4; ++k) { const u32x2 w = *(const u32x2*)(y + yrow[k] + idx);
;             a.x += gk[k] * __uint_as_float(w.x << 16); a.y += gk[k] * __uint_as_float(w.x & 0xffff0000u); a.z += gk[k] * __uint_as_float(w.y << 16); a.w += gk[k] * __uint_as_float(w.y & 0xffff0000u); }
;         v[j] = a; ss += a.x * a.x + a.y * a.y + a.z * a.z + a.w * a.w;
.Lp10_noidx:
	s_waitcnt vmcnt(0)
	v_lshlrev_b32_e32 v148, 16, v84
	v_and_b32_e32 v149, 0xffff0000, v84
	v_lshlrev_b32_e32 v150, 16, v85
	v_and_b32_e32 v151, 0xffff0000, v85
	v_lshlrev_b32_e32 v152, 16, v86
	v_and_b32_e32 v153, 0xffff0000, v86
	v_lshlrev_b32_e32 v154, 16, v87
	v_and_b32_e32 v155, 0xffff0000, v87
	v_fmac_f32_e32 v52, s36, v148
	v_fmac_f32_e32 v53, s36, v149
	v_fmac_f32_e32 v54, s36, v150
	v_fmac_f32_e32 v55, s36, v151
	v_fmac_f32_e32 v56, s36, v152
	v_fmac_f32_e32 v57, s36, v153
	v_fmac_f32_e32 v58, s36, v154
	v_fmac_f32_e32 v59, s36, v155
	v_lshlrev_b32_e32 v148, 16, v100
	v_and_b32_e32 v149, 0xffff0000, v100
	v_lshlrev_b32_e32 v150, 16, v101
	v_and_b32_e32 v151, 0xffff0000, v101
	v_lshlrev_b32_e32 v152, 16, v102
	v_and_b32_e32 v153, 0xffff0000, v102
	v_lshlrev_b32_e32 v154, 16, v103
	v_and_b32_e32 v155, 0xffff0000, v103
	v_fmac_f32_e32 v52, s37, v148
	v_fmac_f32_e32 v53, s37, v149
	v_fmac_f32_e32 v54, s37, v150
	v_fmac_f32_e32 v55, s37, v151
	v_fmac_f32_e32 v56, s37, v152
	v_fmac_f32_e32 v57, s37, v153
	v_fmac_f32_e32 v58, s37, v154
	v_fmac_f32_e32 v59, s37, v155
	v_lshlrev_b32_e32 v148, 16, v116
	v_and_b32_e32 v149, 0xffff0000, v116
	v_lshlrev_b32_e32 v150, 16, v117
	v_and_b32_e32 v151, 0xffff0000, v117
	v_lshlrev_b32_e32 v152, 16, v118
	v_and_b32_e32 v153, 0xffff0000, v118
	v_lshlrev_b32_e32 v154, 16, v119
	v_and_b32_e32 v155, 0xffff0000, v119
	v_fmac_f32_e32 v52, s38, v148
	v_fmac_f32_e32 v53, s38, v149
	v_fmac_f32_e32 v54, s38, v150
	v_fmac_f32_e32 v55, s38, v151
	v_fmac_f32_e32 v56, s38, v152
	v_fmac_f32_e32 v57, s38, v153
	v_fmac_f32_e32 v58, s38, v154
	v_fmac_f32_e32 v59, s38, v155
	v_lshlrev_b32_e32 v148, 16, v132
	v_and_b32_e32 v149, 0xffff0000, v132
	v_lshlrev_b32_e32 v150, 16, v133
	v_and_b32_e32 v151, 0xffff0000, v133
	v_lshlrev_b32_e32 v152, 16, v134
	v_and_b32_e32 v153, 0xffff0000, v134
	v_lshlrev_b32_e32 v154, 16, v135
	v_and_b32_e32 v155, 0xffff0000, v135
	v_fmac_f32_e32 v52, s39, v148
	v_fmac_f32_e32 v53, s39, v149
	v_fmac_f32_e32 v54, s39, v150
	v_fmac_f32_e32 v55, s39, v151
	v_fmac_f32_e32 v56, s39, v152
	v_fmac_f32_e32 v57, s39, v153
	v_fmac_f32_e32 v58, s39, v154
	v_fmac_f32_e32 v59, s39, v155
	v_lshlrev_b32_e32 v148, 16, v88
	v_and_b32_e32 v149, 0xffff0000, v88
	v_lshlrev_b32_e32 v150, 16, v89
	v_and_b32_e32 v151, 0xffff0000, v89
	v_lshlrev_b32_e32 v152, 16, v90
	v_and_b32_e32 v153, 0xffff0000, v90
	v_lshlrev_b32_e32 v154, 16, v91
	v_and_b32_e32 v155, 0xffff0000, v91
	v_fmac_f32_e32 v60, s36, v148
	v_fmac_f32_e32 v61, s36, v149
	v_fmac_f32_e32 v62, s36, v150
	v_fmac_f32_e32 v63, s36, v151
	v_fmac_f32_e32 v64, s36, v152
	v_fmac_f32_e32 v65, s36, v153
	v_fmac_f32_e32 v66, s36, v154
	v_fmac_f32_e32 v67, s36, v155
	v_lshlrev_b32_e32 v148, 16, v104
	v_and_b32_e32 v149, 0xffff0000, v104
	v_lshlrev_b32_e32 v150, 16, v105
	v_and_b32_e32 v151, 0xffff0000, v105
	v_lshlrev_b32_e32 v152, 16, v106
	v_and_b32_e32 v153, 0xffff0000, v106
	v_lshlrev_b32_e32 v154, 16, v107
	v_and_b32_e32 v155, 0xffff0000, v107
	v_fmac_f32_e32 v60, s37, v148
	v_fmac_f32_e32 v61, s37, v149
	v_fmac_f32_e32 v62, s37, v150
	v_fmac_f32_e32 v63, s37, v151
	v_fmac_f32_e32 v64, s37, v152
	v_fmac_f32_e32 v65, s37, v153
	v_fmac_f32_e32 v66, s37, v154
	v_fmac_f32_e32 v67, s37, v155
	v_lshlrev_b32_e32 v148, 16, v120
	v_and_b32_e32 v149, 0xffff0000, v120
	v_lshlrev_b32_e32 v150, 16, v121
	v_and_b32_e32 v151, 0xffff0000, v121
	v_lshlrev_b32_e32 v152, 16, v122
	v_and_b32_e32 v153, 0xffff0000, v122
	v_lshlrev_b32_e32 v154, 16, v123
	v_and_b32_e32 v155, 0xffff0000, v123
	v_fmac_f32_e32 v60, s38, v148
	v_fmac_f32_e32 v61, s38, v149
	v_fmac_f32_e32 v62, s38, v150
	v_fmac_f32_e32 v63, s38, v151
	v_fmac_f32_e32 v64, s38, v152
	v_fmac_f32_e32 v65, s38, v153
	v_fmac_f32_e32 v66, s38, v154
	v_fmac_f32_e32 v67, s38, v155
	v_lshlrev_b32_e32 v148, 16, v136
	v_and_b32_e32 v149, 0xffff0000, v136
	v_lshlrev_b32_e32 v150, 16, v137
	v_and_b32_e32 v151, 0xffff0000, v137
	v_lshlrev_b32_e32 v152, 16, v138
	v_and_b32_e32 v153, 0xffff0000, v138
	v_lshlrev_b32_e32 v154, 16, v139
	v_and_b32_e32 v155, 0xffff0000, v139
	v_fmac_f32_e32 v60, s39, v148
	v_fmac_f32_e32 v61, s39, v149
	v_fmac_f32_e32 v62, s39, v150
	v_fmac_f32_e32 v63, s39, v151
	v_fmac_f32_e32 v64, s39, v152
	v_fmac_f32_e32 v65, s39, v153
	v_fmac_f32_e32 v66, s39, v154
	v_fmac_f32_e32 v67, s39, v155
	v_lshlrev_b32_e32 v148, 16, v92
	v_and_b32_e32 v149, 0xffff0000, v92
	v_lshlrev_b32_e32 v150, 16, v93
	v_and_b32_e32 v151, 0xffff0000, v93
	v_lshlrev_b32_e32 v152, 16, v94
	v_and_b32_e32 v153, 0xffff0000, v94
	v_lshlrev_b32_e32 v154, 16, v95
	v_and_b32_e32 v155, 0xffff0000, v95
	v_fmac_f32_e32 v68, s36, v148
	v_fmac_f32_e32 v69, s36, v149
	v_fmac_f32_e32 v70, s36, v150
	v_fmac_f32_e32 v71, s36, v151
	v_fmac_f32_e32 v72, s36, v152
	v_fmac_f32_e32 v73, s36, v153
	v_fmac_f32_e32 v74, s36, v154
	v_fmac_f32_e32 v75, s36, v155
	v_lshlrev_b32_e32 v148, 16, v108
	v_and_b32_e32 v149, 0xffff0000, v108
	v_lshlrev_b32_e32 v150, 16, v109
	v_and_b32_e32 v151, 0xffff0000, v109
	v_lshlrev_b32_e32 v152, 16, v110
	v_and_b32_e32 v153, 0xffff0000, v110
	v_lshlrev_b32_e32 v154, 16, v111
	v_and_b32_e32 v155, 0xffff0000, v111
	v_fmac_f32_e32 v68, s37, v148
	v_fmac_f32_e32 v69, s37, v149
	v_fmac_f32_e32 v70, s37, v150
	v_fmac_f32_e32 v71, s37, v151
	v_fmac_f32_e32 v72, s37, v152
	v_fmac_f32_e32 v73, s37, v153
	v_fmac_f32_e32 v74, s37, v154
	v_fmac_f32_e32 v75, s37, v155
	v_lshlrev_b32_e32 v148, 16, v124
	v_and_b32_e32 v149, 0xffff0000, v124
	v_lshlrev_b32_e32 v150, 16, v125
	v_and_b32_e32 v151, 0xffff0000, v125
	v_lshlrev_b32_e32 v152, 16, v126
	v_and_b32_e32 v153, 0xffff0000, v126
	v_lshlrev_b32_e32 v154, 16, v127
	v_and_b32_e32 v155, 0xffff0000, v127
; __device__ __forceinline__ void combine_row(int m, int lane, const float* __restrict__ h1, const bf16* __restrict__ y, const unsigned* __restrict__ cnt, const int* __restrict__ tok_e, const int* __restrict__ tok_p, ...
;     ...
; #pragma unroll
;     for (int j = 0; j < 8; ++j) {
;         const int idx = j * 256 + lane * 4;
;         f32x4 a = *(const f32x4*)(h1 + (size_t)m * D + idx);
; #pragma unroll
;         for (int k = 0; k < 4; ++k) { const u32x2 w = *(const u32x2*)(y + yrow[k] + idx);
;             a.x += gk[k] * __uint_as_float(w.x << 16); a.y += gk[k] * __uint_as_float(w.x & 0xffff0000u); a.z += gk[k] * __uint_as_float(w.y << 16); a.w += gk[k] * __uint_as_float(w.y & 0xffff0000u); }
;         v[j] = a; ss += a.x * a.x + a.y * a.y + a.z * a.z + a.w * a.w;
;     }
;     const float rstd = rsqrtf(wave_sum(ss) * (1.f / D) + EPS);
; #pragma unroll
;     for (int j = 0; j < 8; ++j) { const int idx = j * 256 + lane * 4; const f32x4 gg = *(const f32x4*)(g_final + idx);
;         *(f32x4*)(out + (size_t)m * D + idx) = (f32x4){v[j].x * rstd * gg.x, v[j].y * rstd * gg.y, v[j].z * rstd * gg.z, v[j].w * rstd * gg.w}; }
	v_fmac_f32_e32 v68, s38, v148
	v_fmac_f32_e32 v69, s38, v149
	v_fmac_f32_e32 v70, s38, v150
	v_fmac_f32_e32 v71, s38, v151
	v_fmac_f32_e32 v72, s38, v152
	v_fmac_f32_e32 v73, s38, v153
	v_fmac_f32_e32 v74, s38, v154
	v_fmac_f32_e32 v75, s38, v155
	v_lshlrev_b32_e32 v148, 16, v140
	v_and_b32_e32 v149, 0xffff0000, v140
	v_lshlrev_b32_e32 v150, 16, v141
	v_and_b32_e32 v151, 0xffff0000, v141
	v_lshlrev_b32_e32 v152, 16, v142
	v_and_b32_e32 v153, 0xffff0000, v142
	v_lshlrev_b32_e32 v154, 16, v143
	v_and_b32_e32 v155, 0xffff0000, v143
	v_fmac_f32_e32 v68, s39, v148
	v_fmac_f32_e32 v69, s39, v149
	v_fmac_f32_e32 v70, s39, v150
	v_fmac_f32_e32 v71, s39, v151
	v_fmac_f32_e32 v72, s39, v152
	v_fmac_f32_e32 v73, s39, v153
	v_fmac_f32_e32 v74, s39, v154
	v_fmac_f32_e32 v75, s39, v155
	v_lshlrev_b32_e32 v148, 16, v96
	v_and_b32_e32 v149, 0xffff0000, v96
	v_lshlrev_b32_e32 v150, 16, v97
	v_and_b32_e32 v151, 0xffff0000, v97
	v_lshlrev_b32_e32 v152, 16, v98
	v_and_b32_e32 v153, 0xffff0000, v98
	v_lshlrev_b32_e32 v154, 16, v99
	v_and_b32_e32 v155, 0xffff0000, v99
	v_fmac_f32_e32 v76, s36, v148
	v_fmac_f32_e32 v77, s36, v149
	v_fmac_f32_e32 v78, s36, v150
	v_fmac_f32_e32 v79, s36, v151
	v_fmac_f32_e32 v80, s36, v152
	v_fmac_f32_e32 v81, s36, v153
	v_fmac_f32_e32 v82, s36, v154
	v_fmac_f32_e32 v83, s36, v155
	v_lshlrev_b32_e32 v148, 16, v112
	v_and_b32_e32 v149, 0xffff0000, v112
	v_lshlrev_b32_e32 v150, 16, v113
	v_and_b32_e32 v151, 0xffff0000, v113
	v_lshlrev_b32_e32 v152, 16, v114
	v_and_b32_e32 v153, 0xffff0000, v114
	v_lshlrev_b32_e32 v154, 16, v115
	v_and_b32_e32 v155, 0xffff0000, v115
	v_fmac_f32_e32 v76, s37, v148
	v_fmac_f32_e32 v77, s37, v149
	v_fmac_f32_e32 v78, s37, v150
	v_fmac_f32_e32 v79, s37, v151
	v_fmac_f32_e32 v80, s37, v152
	v_fmac_f32_e32 v81, s37, v153
	v_fmac_f32_e32 v82, s37, v154
	v_fmac_f32_e32 v83, s37, v155
	v_lshlrev_b32_e32 v148, 16, v128
	v_and_b32_e32 v149, 0xffff0000, v128
	v_lshlrev_b32_e32 v150, 16, v129
	v_and_b32_e32 v151, 0xffff0000, v129
	v_lshlrev_b32_e32 v152, 16, v130
	v_and_b32_e32 v153, 0xffff0000, v130
	v_lshlrev_b32_e32 v154, 16, v131
	v_and_b32_e32 v155, 0xffff0000, v131
	v_fmac_f32_e32 v76, s38, v148
	v_fmac_f32_e32 v77, s38, v149
	v_fmac_f32_e32 v78, s38, v150
	v_fmac_f32_e32 v79, s38, v151
	v_fmac_f32_e32 v80, s38, v152
	v_fmac_f32_e32 v81, s38, v153
	v_fmac_f32_e32 v82, s38, v154
	v_fmac_f32_e32 v83, s38, v155
	v_lshlrev_b32_e32 v148, 16, v144
	v_and_b32_e32 v149, 0xffff0000, v144
	v_lshlrev_b32_e32 v150, 16, v145
	v_and_b32_e32 v151, 0xffff0000, v145
	v_lshlrev_b32_e32 v152, 16, v146
	v_and_b32_e32 v153, 0xffff0000, v146
	v_lshlrev_b32_e32 v154, 16, v147
	v_and_b32_e32 v155, 0xffff0000, v147
	v_fmac_f32_e32 v76, s39, v148
	v_fmac_f32_e32 v77, s39, v149
	v_fmac_f32_e32 v78, s39, v150
	v_fmac_f32_e32 v79, s39, v151
	v_fmac_f32_e32 v80, s39, v152
	v_fmac_f32_e32 v81, s39, v153
	v_fmac_f32_e32 v82, s39, v154
	v_fmac_f32_e32 v83, s39, v155
	v_mul_f32_e32 v156, v52, v52
	v_fmac_f32_e32 v156, v53, v53
	v_fmac_f32_e32 v156, v54, v54
	v_fmac_f32_e32 v156, v55, v55
	v_fmac_f32_e32 v156, v56, v56
	v_fmac_f32_e32 v156, v57, v57
	v_fmac_f32_e32 v156, v58, v58
	v_fmac_f32_e32 v156, v59, v59
	v_fmac_f32_e32 v156, v60, v60
	v_fmac_f32_e32 v156, v61, v61
	v_fmac_f32_e32 v156, v62, v62
	v_fmac_f32_e32 v156, v63, v63
	v_fmac_f32_e32 v156, v64, v64
	v_fmac_f32_e32 v156, v65, v65
	v_fmac_f32_e32 v156, v66, v66
	v_fmac_f32_e32 v156, v67, v67
	v_fmac_f32_e32 v156, v68, v68
	v_fmac_f32_e32 v156, v69, v69
	v_fmac_f32_e32 v156, v70, v70
	v_fmac_f32_e32 v156, v71, v71
	v_fmac_f32_e32 v156, v72, v72
	v_fmac_f32_e32 v156, v73, v73
	v_fmac_f32_e32 v156, v74, v74
	v_fmac_f32_e32 v156, v75, v75
	v_fmac_f32_e32 v156, v76, v76
	v_fmac_f32_e32 v156, v77, v77
	v_fmac_f32_e32 v156, v78, v78
	v_fmac_f32_e32 v156, v79, v79
	v_fmac_f32_e32 v156, v80, v80
	v_fmac_f32_e32 v156, v81, v81
	v_fmac_f32_e32 v156, v82, v82
	v_fmac_f32_e32 v156, v83, v83
	s_nop 1
	v_add_f32_dpp v156, v156, v156 quad_perm:[1,0,3,2] row_mask:0xf bank_mask:0xf
	s_nop 1
	v_add_f32_dpp v156, v156, v156 quad_perm:[2,3,0,1] row_mask:0xf bank_mask:0xf
	s_nop 1
	v_add_f32_dpp v156, v156, v156 row_half_mirror row_mask:0xf bank_mask:0xf
	s_nop 1
	v_add_f32_dpp v156, v156, v156 row_mirror row_mask:0xf bank_mask:0xf
	s_nop 1
	v_add_f32_dpp v156, v156, v156 row_bcast:15 row_mask:0xa bank_mask:0xf
	s_nop 1
	v_add_f32_dpp v156, v156, v156 row_bcast:31 row_mask:0xc bank_mask:0xf
	s_nop 1
	v_readlane_b32 s60, v156, 63
	s_nop 1
	v_mov_b32_e32 v158, s60
	v_fmamk_f32 v158, v158, 0x3a000000, v157
	v_rsq_f32_e32 v158, v158
	s_nop 0
	v_mov_b32_e32 v159, v158
	v_pk_mul_f32 v[52:53], v[52:53], v[158:159]
	v_pk_mul_f32 v[54:55], v[54:55], v[158:159]
	v_pk_mul_f32 v[56:57], v[56:57], v[158:159]
	v_pk_mul_f32 v[58:59], v[58:59], v[158:159]
	v_pk_mul_f32 v[60:61], v[60:61], v[158:159]
	v_pk_mul_f32 v[62:63], v[62:63], v[158:159]
	v_pk_mul_f32 v[64:65], v[64:65], v[158:159]
	v_pk_mul_f32 v[66:67], v[66:67], v[158:159]
	v_pk_mul_f32 v[68:69], v[68:69], v[158:159]
	v_pk_mul_f32 v[70:71], v[70:71], v[158:159]
	v_pk_mul_f32 v[72:73], v[72:73], v[158:159]
	v_pk_mul_f32 v[74:75], v[74:75], v[158:159]
	v_pk_mul_f32 v[76:77], v[76:77], v[158:159]
	v_pk_mul_f32 v[78:79], v[78:79], v[158:159]
	v_pk_mul_f32 v[80:81], v[80:81], v[158:159]
	v_pk_mul_f32 v[82:83], v[82:83], v[158:159]
	v_pk_mul_f32 v[52:53], v[52:53], v[8:9]
	v_pk_mul_f32 v[54:55], v[54:55], v[10:11]
	v_pk_mul_f32 v[56:57], v[56:57], v[12:13]
	v_pk_mul_f32 v[58:59], v[58:59], v[14:15]
	v_pk_mul_f32 v[60:61], v[60:61], v[16:17]
	v_pk_mul_f32 v[62:63], v[62:63], v[18:19]
	v_pk_mul_f32 v[64:65], v[64:65], v[20:21]
	v_pk_mul_f32 v[66:67], v[66:67], v[22:23]
	v_pk_mul_f32 v[68:69], v[68:69], v[24:25]
	v_pk_mul_f32 v[70:71], v[70:71], v[26:27]
	v_pk_mul_f32 v[72:73], v[72:73], v[28:29]
	v_pk_mul_f32 v[74:75], v[74:75], v[30:31]
	v_pk_mul_f32 v[76:77], v[76:77], v[32:33]
	v_pk_mul_f32 v[78:79], v[78:79], v[34:35]
	v_pk_mul_f32 v[80:81], v[80:81], v[36:37]
	v_pk_mul_f32 v[82:83], v[82:83], v[38:39]
	global_store_dwordx4 v2, v[52:55], s[50:51]
	global_store_dwordx4 v2, v[56:59], s[50:51] offset:16
	global_store_dwordx4 v2, v[60:63], s[50:51] offset:2048
	global_store_dwordx4 v2, v[64:67], s[50:51] offset:2064
	global_store_dwordx4 v2, v[68:71], s[26:27]
	global_store_dwordx4 v2, v[72:75], s[26:27] offset:16
	global_store_dwordx4 v2, v[76:79], s[26:27] offset:2048
	global_store_dwordx4 v2, v[80:83], s[26:27] offset:2064
	s_cmp_eq_u32 s65, 0
	s_cbranch_scc1 .LBB0_1580
; __device__ __forceinline__ void combine_row(int m, int lane, const float* __restrict__ h1, const bf16* __restrict__ y, const unsigned* __restrict__ cnt, const int* __restrict__ tok_e, const int* __restrict__ tok_p, ...
;     ...
; #pragma unroll
;     for (int k = 0; k < 4; ++k) {
;         const int e = tok_e[m * 4 + k]; const int off = (int)cnt[e];
;         yrow[k] = (size_t)(off + tok_p[m * 4 + k]) * D; gk[k] = gate[m * 4 + k];
	v_readfirstlane_b32 s28, v40
	v_readfirstlane_b32 s29, v41
	v_readfirstlane_b32 s30, v42
	v_readfirstlane_b32 s31, v43
	v_readfirstlane_b32 s32, v44
	v_readfirstlane_b32 s33, v45
	v_readfirstlane_b32 s34, v46
	v_readfirstlane_b32 s35, v47
	v_readfirstlane_b32 s36, v48
	v_readfirstlane_b32 s37, v49
	v_readfirstlane_b32 s38, v50
	v_readfirstlane_b32 s39, v51
	s_nop 3
	v_readlane_b32 s60, v6, s28
	v_readlane_b32 s61, v6, s29
	v_readlane_b32 s62, v6, s30
	v_readlane_b32 s63, v6, s31
	s_add_i32 s60, s60, s32
	s_lshl_b32 s60, s60, 12
	s_add_u32 s40, s24, s60
	s_addc_u32 s41, s25, 0
	s_add_i32 s61, s61, s33
	s_lshl_b32 s61, s61, 12
	s_add_u32 s42, s24, s61
	s_addc_u32 s43, s25, 0
	s_add_i32 s62, s62, s34
	s_lshl_b32 s62, s62, 12
	s_add_u32 s44, s24, s62
	s_addc_u32 s45, s25, 0
	s_add_i32 s63, s63, s35
	s_lshl_b32 s63, s63, 12
	s_add_u32 s46, s24, s63
	s_addc_u32 s47, s25, 0
	s_lshl_b32 s60, s8, 13
	s_add_u32 s48, s16, s60
	s_addc_u32 s49, s17, 0
	s_add_u32 s58, s48, 0x1000
	s_addc_u32 s59, s49, 0
	s_add_u32 s50, s6, s60
	s_addc_u32 s51, s7, 0
	s_add_u32 s26, s50, 0x1000
	s_addc_u32 s27, s51, 0
	s_branch .Lp10_loop
